# ph_slots: per-token routed assignments batched (4 wide loads, 8 rank atomics back to back, then 16 stores) instead of 8 serial load->atomic->store steps
# baseline (speedup 1.0000x reference)
.LBB0_3351:
	v_ashrrev_i32_e32 v7, 31, v6
	v_lshlrev_b64 v[10:11], 5, v[6:7]
	v_lshl_add_u64 v[8:9], s[6:7], 0, v[10:11]
	global_load_dwordx4 v[28:31], v[8:9], off
	global_load_dwordx4 v[32:35], v[8:9], off offset:16
	v_lshl_add_u64 v[8:9], s[8:9], 0, v[10:11]
	global_load_dwordx4 v[36:39], v[8:9], off
	global_load_dwordx4 v[40:43], v[8:9], off offset:16
	v_lshrrev_b32_e32 v7, 18, v7
	v_add_u32_e32 v7, v6, v7
	v_ashrrev_i32_e32 v7, 14, v7
	v_lshl_or_b32 v24, v7, 8, v12
	v_mad_i32_i24 v26, v7, s12, 0
	v_mul_i32_i24_e32 v27, 0x28000, v7
	v_mul_i32_i24_e32 v25, 0x4000, v7
	v_lshlrev_b32_e32 v8, 3, v25
	v_sub_u32_e32 v9, v3, v8
	v_add_u32_e32 v3, s5, v3
	ds_read_b32 v60, v26 offset:256
	s_waitcnt vmcnt(2)
	v_add_u32_e32 v14, v24, v28
	v_ashrrev_i32_e32 v15, 31, v14
	v_lshl_add_u64 v[14:15], v[14:15], 2, s[2:3]
	global_atomic_add v44, v[14:15], v13, off sc0
	v_lshl_add_u32 v14, v28, 2, v26
	ds_read_b32 v52, v14
	v_add_u32_e32 v14, v24, v29
	v_ashrrev_i32_e32 v15, 31, v14
	v_lshl_add_u64 v[14:15], v[14:15], 2, s[2:3]
	global_atomic_add v45, v[14:15], v13, off sc0
	v_lshl_add_u32 v14, v29, 2, v26
	ds_read_b32 v53, v14
	v_add_u32_e32 v14, v24, v30
	v_ashrrev_i32_e32 v15, 31, v14
	v_lshl_add_u64 v[14:15], v[14:15], 2, s[2:3]
	global_atomic_add v46, v[14:15], v13, off sc0
	v_lshl_add_u32 v14, v30, 2, v26
	ds_read_b32 v54, v14
	v_add_u32_e32 v14, v24, v31
	v_ashrrev_i32_e32 v15, 31, v14
	v_lshl_add_u64 v[14:15], v[14:15], 2, s[2:3]
	global_atomic_add v47, v[14:15], v13, off sc0
	v_lshl_add_u32 v14, v31, 2, v26
	ds_read_b32 v55, v14
	v_add_u32_e32 v14, v24, v32
	v_ashrrev_i32_e32 v15, 31, v14
	v_lshl_add_u64 v[14:15], v[14:15], 2, s[2:3]
	global_atomic_add v48, v[14:15], v13, off sc0
	v_lshl_add_u32 v14, v32, 2, v26
	ds_read_b32 v56, v14
	v_add_u32_e32 v14, v24, v33
	v_ashrrev_i32_e32 v15, 31, v14
	v_lshl_add_u64 v[14:15], v[14:15], 2, s[2:3]
	global_atomic_add v49, v[14:15], v13, off sc0
	v_lshl_add_u32 v14, v33, 2, v26
	ds_read_b32 v57, v14
	v_add_u32_e32 v14, v24, v34
	v_ashrrev_i32_e32 v15, 31, v14
	v_lshl_add_u64 v[14:15], v[14:15], 2, s[2:3]
	global_atomic_add v50, v[14:15], v13, off sc0
	v_lshl_add_u32 v14, v34, 2, v26
	ds_read_b32 v58, v14
	v_add_u32_e32 v14, v24, v35
	v_ashrrev_i32_e32 v15, 31, v14
	v_lshl_add_u64 v[14:15], v[14:15], 2, s[2:3]
	global_atomic_add v51, v[14:15], v13, off sc0
	v_lshl_add_u32 v14, v35, 2, v26
	ds_read_b32 v59, v14
	s_waitcnt vmcnt(0) lgkmcnt(0)
	v_lshlrev_b32_e32 v14, 8, v52
	v_add3_u32 v14, v44, v27, v14
	v_ashrrev_i32_e32 v15, 31, v14
	v_lshl_add_u64 v[16:17], v[14:15], 2, s[26:27]
	v_lshl_add_u64 v[18:19], v[14:15], 3, s[28:29]
	global_store_dword v[16:17], v6, off
	v_mov_b32_e32 v20, v36
	v_add_u32_e32 v21, -7, v9
	global_store_dwordx2 v[18:19], v[20:21], off
	v_lshlrev_b32_e32 v14, 8, v53
	v_add3_u32 v14, v45, v27, v14
	v_ashrrev_i32_e32 v15, 31, v14
	v_lshl_add_u64 v[16:17], v[14:15], 2, s[26:27]
	v_lshl_add_u64 v[18:19], v[14:15], 3, s[28:29]
	global_store_dword v[16:17], v6, off
	v_mov_b32_e32 v20, v37
	v_add_u32_e32 v21, -6, v9
	global_store_dwordx2 v[18:19], v[20:21], off
	v_lshlrev_b32_e32 v14, 8, v54
	v_add3_u32 v14, v46, v27, v14
	v_ashrrev_i32_e32 v15, 31, v14
	v_lshl_add_u64 v[16:17], v[14:15], 2, s[26:27]
	v_lshl_add_u64 v[18:19], v[14:15], 3, s[28:29]
	global_store_dword v[16:17], v6, off
	v_mov_b32_e32 v20, v38
	v_add_u32_e32 v21, -5, v9
	global_store_dwordx2 v[18:19], v[20:21], off
	v_lshlrev_b32_e32 v14, 8, v55
	v_add3_u32 v14, v47, v27, v14
	v_ashrrev_i32_e32 v15, 31, v14
	v_lshl_add_u64 v[16:17], v[14:15], 2, s[26:27]
	v_lshl_add_u64 v[18:19], v[14:15], 3, s[28:29]
	global_store_dword v[16:17], v6, off
	v_mov_b32_e32 v20, v39
	v_add_u32_e32 v21, -4, v9
	global_store_dwordx2 v[18:19], v[20:21], off
	v_lshlrev_b32_e32 v14, 8, v56
	v_add3_u32 v14, v48, v27, v14
	v_ashrrev_i32_e32 v15, 31, v14
	v_lshl_add_u64 v[16:17], v[14:15], 2, s[26:27]
	v_lshl_add_u64 v[18:19], v[14:15], 3, s[28:29]
	global_store_dword v[16:17], v6, off
	v_mov_b32_e32 v20, v40
	v_add_u32_e32 v21, -3, v9
	global_store_dwordx2 v[18:19], v[20:21], off
	v_lshlrev_b32_e32 v14, 8, v57
	v_add3_u32 v14, v49, v27, v14
	v_ashrrev_i32_e32 v15, 31, v14
	v_lshl_add_u64 v[16:17], v[14:15], 2, s[26:27]
	v_lshl_add_u64 v[18:19], v[14:15], 3, s[28:29]
	global_store_dword v[16:17], v6, off
	v_mov_b32_e32 v20, v41
	v_add_u32_e32 v21, -2, v9
	global_store_dwordx2 v[18:19], v[20:21], off
	v_lshlrev_b32_e32 v14, 8, v58
	v_add3_u32 v14, v50, v27, v14
	v_ashrrev_i32_e32 v15, 31, v14
	v_lshl_add_u64 v[16:17], v[14:15], 2, s[26:27]
	v_lshl_add_u64 v[18:19], v[14:15], 3, s[28:29]
	global_store_dword v[16:17], v6, off
	v_mov_b32_e32 v20, v42
	v_add_u32_e32 v21, -1, v9
	global_store_dwordx2 v[18:19], v[20:21], off
	v_lshlrev_b32_e32 v14, 8, v59
	v_add3_u32 v14, v51, v27, v14
	v_ashrrev_i32_e32 v15, 31, v14
	v_lshl_add_u64 v[16:17], v[14:15], 2, s[26:27]
	v_lshl_add_u64 v[18:19], v[14:15], 3, s[28:29]
	global_store_dword v[16:17], v6, off
	v_mov_b32_e32 v20, v43
	v_add_u32_e32 v21, 0, v9
	global_store_dwordx2 v[18:19], v[20:21], off
	v_lshlrev_b32_e32 v10, 8, v60
	v_mad_i32_i24 v7, v7, s13, v10
	v_sub_u32_e32 v7, v7, v25
	v_add_u32_e32 v10, v6, v7
	v_ashrrev_i32_e32 v11, 31, v10
	v_lshl_add_u64 v[14:15], v[10:11], 2, s[26:27]
	v_lshl_add_u64 v[10:11], v[10:11], 3, s[28:29]
	v_mov_b32_e32 v5, v6
	global_store_dword v[14:15], v6, off
	global_store_dwordx2 v[10:11], v[4:5], off
	v_add_u32_e32 v6, s4, v6
	v_cmp_lt_i32_e32 vcc, s14, v6
	s_or_b64 s[10:11], vcc, s[10:11]
	s_andn2_b64 exec, exec, s[10:11]
	s_cbranch_execnz .LBB0_3351
	s_nop 0
	s_nop 0
	s_nop 0
	s_nop 0
	s_nop 0
	s_nop 0
	s_nop 0
	s_or_b64 exec, exec, s[10:11]
	s_mov_b64 s[6:7], 0
	s_movk_i32 s5, 0x7fff
	v_mov_b32_e32 v4, 0
	v_mov_b32_e32 v5, -1
	s_branch .LBB0_3354
